# MoE GEMM phases: per-tile expert lookup via v_readlane from a 3-VGPR table loaded once per phase (was global_load + s_waitcnt vmcnt(0) draining all stores at every tile boundary); on top of v031
# speedup vs baseline: 1.0206x; 1.0069x over previous
.LBB0_1477:
	s_cmp_lt_i32 s30, 17
	s_cselect_b64 s[6:7], -1, 0
	s_and_b64 s[0:1], s[6:7], s[0:1]
	s_andn2_b64 vcc, exec, s[0:1]
	s_cbranch_vccnz .LBB0_1504
	v_mov_b32_e32 v1, 0x7e8000
	global_load_dword v1, v1, s[28:29] offset:1020
	v_lshlrev_b32_e32 v240, 2, v218
	v_add_u32_e32 v240, 0x7e8000, v240
	global_load_dword v241, v240, s[28:29] offset:256
	global_load_dword v242, v240, s[28:29] offset:512
	global_load_dword v240, v240, s[28:29]
	v_readfirstlane_b32 s2, v0
	s_waitcnt vmcnt(0)
	v_readfirstlane_b32 s3, v1
	s_mul_i32 s0, s3, 44
	s_cmp_ge_i32 s96, s0
	s_cbranch_scc1 .LBB0_1504
	s_ashr_i32 s33, s96, 31
	s_lshr_b32 s1, s33, 29
	s_add_i32 s10, s96, s1
	s_and_b32 s1, s10, -8
	s_sub_i32 s8, s96, s1
	s_ashr_i32 s1, s0, 31
	s_lshr_b32 s4, s1, 29
	s_add_i32 s4, s0, s4
	s_ashr_i32 s35, s4, 3
	s_and_b32 s4, s4, -8
	s_sub_i32 s43, s0, s4
	s_add_i32 s45, s35, 1
	s_cmp_ge_i32 s8, s43
	s_mul_i32 s58, s45, s43
	s_cbranch_scc0 .LBB0_1481
	s_sub_i32 s4, s8, s43
	s_mul_i32 s4, s4, s35
	s_add_i32 s11, s4, s58
	s_cbranch_execz .LBB0_1482
	s_branch .LBB0_1483

.LBB0_1494:
	s_nop 0
	v_cndmask_b32_e64 v4, 0, 1, s[4:5]
	s_ashr_i32 s49, s48, 31
	v_cmp_ne_u32_e64 s[0:1], 1, v4
	s_andn2_b64 vcc, exec, s[4:5]
	v_mov_b64_e32 v[174:175], v[2:3]
	s_cbranch_vccnz .LBB0_1496
	s_and_b32 s98, s48, 63
	s_lshr_b32 s99, s48, 6
	v_readlane_b32 s50, v240, s98
	v_readlane_b32 s51, v241, s98
	s_cmp_eq_u32 s99, 1
	s_cselect_b32 s50, s51, s50
	v_readlane_b32 s51, v242, s98
	s_cmp_eq_u32 s99, 2
	s_cselect_b32 s50, s51, s50
	v_mov_b32_e32 v4, s50
	s_ashr_i32 s47, s46, 31
	s_lshl_b64 s[50:51], s[46:47], 19
	v_mul_hi_i32 v5, v4, s55
	v_mul_lo_u32 v4, v4, s55
	v_lshl_add_u64 v[4:5], s[8:9], 0, v[4:5]
	v_lshl_add_u64 v[174:175], v[4:5], 0, s[50:51]

.LBB0_1554:
	s_cmp_lt_i32 s30, 18
	s_cselect_b64 s[6:7], -1, 0
	s_and_b64 s[0:1], s[6:7], s[0:1]
	s_andn2_b64 vcc, exec, s[0:1]
	s_cbranch_vccnz .LBB0_1575
	v_mov_b32_e32 v1, 0x7e8000
	global_load_dword v1, v1, s[28:29] offset:1020
	v_lshlrev_b32_e32 v240, 2, v218
	v_add_u32_e32 v240, 0x7e8000, v240
	global_load_dword v241, v240, s[28:29] offset:256
	global_load_dword v242, v240, s[28:29] offset:512
	global_load_dword v240, v240, s[28:29]
	v_readfirstlane_b32 s0, v0
	s_waitcnt vmcnt(0)
	v_lshlrev_b32_e32 v162, 3, v1
	v_cmp_ge_i32_e32 vcc, s96, v162
	v_readfirstlane_b32 s3, v1
	s_cbranch_vccnz .LBB0_1575
	s_add_u32 s8, s28, 0x1e400000
	s_addc_u32 s9, s29, 0
	s_ashr_i32 s35, s96, 31
	s_lshr_b32 s2, s35, 29
	s_add_i32 s2, s96, s2
	s_lshr_b32 s1, s0, 6
	s_ashr_i32 s5, s2, 3
	s_and_b32 s2, s2, -8
	s_lshr_b32 s4, s0, 8
	s_lshl_b32 s33, s1, 10
	s_sub_i32 s2, s96, s2
	s_add_i32 s60, s3, 1
	s_cmp_lt_i32 s2, 0
	s_cselect_b32 s10, s60, s3
	s_mul_i32 s2, s10, s2
	s_add_i32 s2, s2, s5
	s_ashr_i32 s5, s2, 31
	s_lshr_b32 s5, s5, 27
	s_add_i32 s5, s2, s5
	s_ashr_i32 s10, s5, 5
	s_lshl_b32 s10, s10, 2
	s_sub_i32 s11, s3, s10
	s_min_i32 s11, s11, 4
	s_abs_i32 s12, s11
	v_cvt_f32_u32_e32 v1, s12
	s_sub_i32 s14, 0, s12
	s_andn2_b32 s5, s5, 31
	s_sub_i32 s5, s2, s5
	v_rcp_iflag_f32_e32 v1, v1
	s_abs_i32 s13, s5
	s_xor_b32 s2, s5, s11
	s_ashr_i32 s2, s2, 31
	v_mul_f32_e32 v1, 0x4f7ffffe, v1
	v_cvt_u32_f32_e32 v1, v1
	v_mov_b32_e32 v165, 0
	v_lshlrev_b32_e32 v164, 4, v0
	v_and_b32_e32 v2, 32, v0
	v_readfirstlane_b32 s15, v1
	s_mul_i32 s14, s14, s15
	s_mul_hi_u32 s14, s15, s14
	s_add_i32 s15, s15, s14
	s_mul_hi_u32 s14, s13, s15
	s_mul_i32 s15, s14, s12
	s_sub_i32 s13, s13, s15
	s_add_i32 s15, s14, 1
	s_sub_i32 s18, s13, s12
	s_cmp_ge_u32 s13, s12
	s_cselect_b32 s14, s15, s14
	s_cselect_b32 s13, s18, s13
	s_add_i32 s15, s14, 1
	s_cmp_ge_u32 s13, s12
	s_cselect_b32 s12, s15, s14
	s_xor_b32 s12, s12, s2
	s_sub_i32 s2, s12, s2
	s_mul_i32 s11, s2, s11
	s_sub_i32 s5, s5, s11
	s_add_i32 s54, s10, s5
	s_ashr_i32 s55, s54, 31
	s_lshl_b64 s[10:11], s[54:55], 2
	s_add_u32 s10, s16, s10
	s_addc_u32 s11, s17, s11
	global_load_dword v1, v165, s[10:11]
	v_bfe_u32 v3, v0, 2, 4
	v_lshrrev_b32_e32 v4, 3, v0
	s_movk_i32 s5, 0x70
	v_bitop3_b32 v11, v164, v2, 48 bitop3:0x6c
	v_and_or_b32 v2, v4, 48, v3
	v_or_b32_e32 v4, 64, v4
	s_mov_b32 s55, 0xb00000
	v_mul_u32_u24_e32 v12, 0x1600, v2
	v_and_or_b32 v2, v4, s5, v3
	v_mul_u32_u24_e32 v13, 0x1600, v2
	v_and_b32_e32 v10, 64, v0
	s_mul_hi_i32 s19, s2, 0x160000
	s_mul_i32 s18, s2, 0x160000
	v_or_b32_e32 v5, v11, v10
	s_add_i32 s61, s33, 0
	s_mov_b64 s[10:11], 0x2000
	v_or_b32_e32 v166, v12, v5
	v_or_b32_e32 v168, v13, v5
	s_add_i32 m0, s61, 0x10000
	s_mov_b64 s[12:13], 0x4000
	s_mul_i32 s20, s54, 0x160000
	s_mov_b64 s[14:15], 0x6000
	s_mul_hi_i32 s5, s54, 0x160000
	v_mov_b32_e32 v167, v165
	v_mov_b32_e32 v169, v165
	s_mov_b32 s65, 0
	s_waitcnt vmcnt(0)
	v_mul_hi_i32 v3, v1, s55
	v_mul_lo_u32 v2, v1, s55
	v_lshl_add_u64 v[2:3], s[8:9], 0, v[2:3]
	v_lshl_add_u64 v[2:3], v[2:3], 0, s[18:19]
	v_lshl_add_u64 v[4:5], v[2:3], 0, v[164:165]
	v_readfirstlane_b32 s18, v2
	v_readfirstlane_b32 s19, v3
	v_lshl_add_u64 v[6:7], v[4:5], 0, s[10:11]
	v_lshl_add_u64 v[8:9], v[4:5], 0, s[12:13]
	v_lshl_add_u64 v[14:15], v[4:5], 0, s[14:15]
	s_nop 1
	global_load_lds_dwordx4 v164, s[18:19]
	s_add_i32 m0, s61, 0x12000
	v_readlane_b32 s18, v254, 56
	global_load_lds_dwordx4 v[6:7], off
	s_add_i32 m0, s61, 0x14000
	v_readlane_b32 s19, v254, 57
	global_load_lds_dwordx4 v[8:9], off
	s_add_i32 m0, s61, 0x16000
	s_add_u32 s56, s18, s20
	s_addc_u32 s57, s19, s5
	s_add_i32 s62, s61, 0x2000
	global_load_lds_dwordx4 v[14:15], off
	s_mov_b32 m0, s61
	s_add_u32 s18, s56, 0xb0000
	global_load_lds_dwordx4 v166, s[56:57]
	s_mov_b32 m0, s62
	s_addc_u32 s19, s57, 0
	s_add_i32 s63, s61, 0x4000
	global_load_lds_dwordx4 v168, s[56:57]
	s_add_i32 s64, s61, 0x6000
	s_mov_b32 m0, s63
	s_cmp_eq_u32 s4, 1
	global_load_lds_dwordx4 v166, s[18:19]
	s_mov_b32 m0, s64
	v_lshl_add_u64 v[8:9], s[56:57], 0, v[166:167]
	global_load_lds_dwordx4 v168, s[18:19]
	v_lshl_add_u64 v[6:7], s[56:57], 0, v[168:169]
	s_cselect_b64 s[18:19], -1, 0
	s_cmp_lg_u32 s4, 1
	s_mov_b64 s[20:21], 0xb0000
	s_cbranch_scc1 .LBB0_1558
	s_barrier

.LBB0_1565:
	s_and_b64 vcc, exec, s[0:1]
	v_mov_b64_e32 v[174:175], v[2:3]
	s_cbranch_vccnz .LBB0_1567
	s_ashr_i32 s53, s52, 31
	s_and_b32 s98, s52, 63
	s_lshr_b32 s99, s52, 6
	v_readlane_b32 s58, v240, s98
	v_readlane_b32 s59, v241, s98
	s_cmp_eq_u32 s99, 1
	s_cselect_b32 s58, s59, s58
	v_readlane_b32 s59, v242, s98
	s_cmp_eq_u32 s99, 2
	s_cselect_b32 s58, s59, s58
	v_mov_b32_e32 v4, s58
	s_mul_hi_i32 s59, s75, 0x160000
	s_mul_i32 s58, s75, 0x160000
	v_mul_hi_i32 v5, v4, s55
	v_mul_lo_u32 v4, v4, s55
	v_lshl_add_u64 v[4:5], s[8:9], 0, v[4:5]
	v_lshl_add_u64 v[174:175], v[4:5], 0, s[58:59]
